# nt (streaming) cache policy on the once-read loads of the two HBM-bound streams: x in the P0 rmsnorm and X3 / YSLOT rows in the final combine
# baseline (speedup 1.0000x reference)
; __device__ __forceinline__ unsigned pk2(float lo, float hi) { const f32x2h v = {lo, hi}; const bf16x2h b = __builtin_convertvector(v, bf16x2h); return __builtin_bit_cast(unsigned, b); }
; __device__ __forceinline__ void s5_tables1_ph(const int WID_, const float* dsk, const S5Tab& T) {
;     ...
;     for (int i = gtid; i < 32 * 512 * 64; i += gsz) {
;         const int c8 = i & 63, row = (i >> 6) & 511, g = i >> 15;
;         const int sp = row >> 4, hp = row & 15, s = c8 >> 1, h0 = (c8 & 1) * 8;
;         const bool on = s <= sp;
;         const float* k = T.Kmat + ((g * 32 + (on ? sp - s : 0)) * 16 + hp) * 16 + h0;
;         const float4 a = *(const float4*)k, b = *(const float4*)(k + 4);
;         const float dd = dsk[g * 16 + hp];
;         float v[8] = {a.x, a.y, a.z, a.w, b.x, b.y, b.z, b.w};
; #pragma unroll
;         for (int e = 0; e < 8; ++e) { if (!on) v[e] = 0.f; if ((row >> 3) == c8 && (row & 7) == e) v[e] += dd; }
;         *(uint4*)(T.BtA + ((size_t)g * 768 + row) * 512 + c8 * 8) = make_uint4(pk2(v[0], v[1]), pk2(v[2], v[3]), pk2(v[4], v[5]), pk2(v[6], v[7]));
;     }
.LBB0_102:
	v_lshrrev_b32_e32 v5, 6, v2
	v_ashrrev_i32_e32 v6, 15, v2
	v_bfe_u32 v25, v2, 6, 4
	v_and_b32_e32 v4, 8, v18
	v_add_u32_e32 v14, s96, v2
	v_add_u32_e32 v15, s33, v2
	v_bfe_u32 v23, v5, 4, 5
	v_bfe_u32 v7, v2, 6, 3
	s_mul_i32 s0, s94, 0x600
	v_lshlrev_b32_e32 v26, 9, v6
	v_lshlrev_b32_e32 v10, 2, v4
	v_lshl_or_b32 v4, v6, 4, v25
	v_bfe_u32 v22, v5, 3, 6
	v_mul_i32_i24_e32 v6, 0x300, v6
	v_lshrrev_b32_e32 v24, 6, v14
	v_ashrrev_i32_e32 v27, 15, v14
	v_bfe_u32 v28, v14, 6, 4
	v_lshrrev_b32_e32 v30, 6, v15
	v_bfe_u32 v12, v15, 6, 9
	v_bfe_u32 v32, v15, 6, 4
	v_bfe_u32 v33, v15, 6, 3
	v_sub_u32_e64 v15, v23, v17 clamp
	v_bfe_u32 v0, v2, 6, 9
	v_mov_b32_e32 v1, v11
	v_add_u32_e32 v19, s0, v2
	v_cmp_eq_u32_e64 s[12:13], 0, v7
	v_cmp_eq_u32_e64 s[14:15], 1, v7
	v_cmp_eq_u32_e64 s[16:17], 2, v7
	v_cmp_eq_u32_e64 s[20:21], 3, v7
	v_cmp_eq_u32_e64 s[22:23], 4, v7
	v_cmp_eq_u32_e64 s[24:25], 5, v7
	v_cmp_eq_u32_e64 s[26:27], 6, v7
	v_cmp_eq_u32_e64 s[28:29], 7, v7
	v_bfe_u32 v2, v14, 6, 9
	v_bfe_u32 v29, v14, 6, 3
	v_add_u32_e32 v31, s96, v14
	v_ashrrev_i32_e32 v5, 31, v4
	v_cmp_eq_u32_e64 s[30:31], v22, v16
	v_ashrrev_i32_e32 v7, 31, v6
	v_bfe_u32 v34, v24, 4, 5
	v_lshlrev_b32_e32 v35, 9, v27
	v_lshl_or_b32 v14, v27, 4, v28
	v_mul_i32_i24_e32 v22, 0x300, v27
	v_lshlrev_b32_e32 v27, 4, v15
	v_lshl_add_u64 v[4:5], v[4:5], 2, s[84:85]
	v_lshl_add_u64 v[0:1], v[6:7], 0, v[0:1]
	v_sub_u32_e64 v6, v34, v17 clamp
	v_or3_b32 v26, v27, v26, v25
	v_mov_b32_e32 v3, v11
	v_cmp_gt_u32_e64 s[50:51], v17, v23
	v_ashrrev_i32_e32 v23, 31, v22
	s_and_b64 s[14:15], s[14:15], s[30:31]
	s_and_b64 s[16:17], s[16:17], s[30:31]
	s_and_b64 s[20:21], s[20:21], s[30:31]
	s_and_b64 s[22:23], s[22:23], s[30:31]
	s_and_b64 s[24:25], s[24:25], s[30:31]
	s_and_b64 s[26:27], s[26:27], s[30:31]
	s_and_b64 s[28:29], s[28:29], s[30:31]
	s_and_b64 s[12:13], s[12:13], s[30:31]
	v_cmp_gt_u32_e64 s[30:31], v17, v34
	global_load_dword v34, v[4:5], off
	v_lshlrev_b64 v[0:1], 10, v[0:1]
	v_lshlrev_b32_e32 v5, 4, v6
	v_lshlrev_b32_e32 v4, 4, v26
	v_bfe_u32 v37, v30, 4, 5
	v_lshl_add_u64 v[2:3], v[22:23], 0, v[2:3]
	v_lshl_add_u64 v[22:23], v[8:9], 0, v[0:1]
	v_or3_b32 v0, v5, v35, v28
	v_ashrrev_i32_e32 v5, 31, v4
	v_ashrrev_i32_e32 v36, 15, v31
	v_sub_u32_e64 v7, v37, v17 clamp
	v_lshlrev_b64 v[26:27], 10, v[2:3]
	v_lshlrev_b32_e32 v0, 4, v0
	v_lshl_add_u64 v[2:3], v[4:5], 2, s[18:19]
	v_bfe_u32 v24, v24, 3, 6
	v_cmp_eq_u32_e64 s[34:35], 0, v29
	v_cmp_eq_u32_e64 s[36:37], 1, v29
	v_cmp_eq_u32_e64 s[38:39], 2, v29
	v_cmp_eq_u32_e64 s[40:41], 3, v29
	v_cmp_eq_u32_e64 s[42:43], 4, v29
	v_cmp_eq_u32_e64 s[44:45], 5, v29
	v_cmp_eq_u32_e64 s[46:47], 6, v29
	v_cmp_eq_u32_e64 s[48:49], 7, v29
	v_lshlrev_b32_e32 v29, 9, v36
	v_lshlrev_b32_e32 v6, 4, v7
	v_ashrrev_i32_e32 v1, 31, v0
	v_lshl_add_u64 v[4:5], v[2:3], 0, v[10:11]
	v_cmp_eq_u32_e64 s[52:53], v24, v16
	v_lshl_or_b32 v24, v36, 4, v32
	v_or3_b32 v32, v6, v29, v32
	v_lshl_add_u64 v[28:29], v[0:1], 2, s[18:19]
	global_load_dwordx4 v[0:3], v[4:5], off nt
	s_nop 0
	global_load_dwordx4 v[4:7], v[4:5], off offset:16 nt
	v_ashrrev_i32_e32 v15, 31, v14
	v_lshl_add_u64 v[28:29], v[28:29], 0, v[10:11]
	v_lshl_add_u64 v[14:15], v[14:15], 2, s[84:85]
	v_ashrrev_i32_e32 v25, 31, v24
	s_and_b64 s[36:37], s[36:37], s[52:53]
	s_and_b64 s[38:39], s[38:39], s[52:53]
	s_and_b64 s[40:41], s[40:41], s[52:53]
	s_and_b64 s[42:43], s[42:43], s[52:53]
	s_and_b64 s[44:45], s[44:45], s[52:53]
	s_and_b64 s[46:47], s[46:47], s[52:53]
	s_and_b64 s[48:49], s[48:49], s[52:53]
	s_and_b64 s[34:35], s[34:35], s[52:53]
	v_lshrrev_b32_e32 v20, 6, v19
	v_mov_b32_e32 v13, v11
	v_bfe_u32 v21, v19, 6, 4
	v_bfe_u32 v30, v30, 3, 6
	v_cmp_eq_u32_e32 vcc, 0, v33
	v_cmp_eq_u32_e64 s[0:1], 1, v33
	v_cmp_eq_u32_e64 s[2:3], 2, v33
	v_cmp_eq_u32_e64 s[4:5], 3, v33
	v_cmp_eq_u32_e64 s[6:7], 4, v33
	v_cmp_eq_u32_e64 s[8:9], 5, v33
	v_cmp_eq_u32_e64 s[10:11], 6, v33
	v_add_u32_e32 v18, s58, v18
	s_waitcnt vmcnt(1)
	v_cndmask_b32_e64 v0, v0, 0, s[50:51]
	v_cndmask_b32_e64 v1, v1, 0, s[50:51]
	v_cndmask_b32_e64 v2, v2, 0, s[50:51]
	v_cndmask_b32_e64 v3, v3, 0, s[50:51]
	s_waitcnt vmcnt(0)
	v_cndmask_b32_e64 v4, v4, 0, s[50:51]
	v_cndmask_b32_e64 v5, v5, 0, s[50:51]
	v_cndmask_b32_e64 v6, v6, 0, s[50:51]
	v_cndmask_b32_e64 v7, v7, 0, s[50:51]
	v_add_f32_e32 v35, v34, v0
	v_add_f32_e32 v38, v34, v1
	v_add_f32_e32 v39, v34, v2
	v_add_f32_e32 v40, v34, v3
	v_add_f32_e32 v41, v34, v4
	v_add_f32_e32 v42, v34, v5
	v_add_f32_e32 v43, v34, v6
	v_add_f32_e32 v34, v34, v7
	v_cndmask_b32_e64 v0, v0, v35, s[12:13]
	v_cndmask_b32_e64 v1, v1, v38, s[14:15]
	v_cndmask_b32_e64 v2, v2, v39, s[16:17]
	v_cndmask_b32_e64 v3, v3, v40, s[20:21]
	v_cndmask_b32_e64 v4, v4, v41, s[22:23]
	v_cndmask_b32_e64 v5, v5, v42, s[24:25]
	v_cndmask_b32_e64 v6, v6, v43, s[26:27]
	v_cndmask_b32_e64 v7, v7, v34, s[28:29]
	v_cvt_pk_bf16_f32 v0, v0, v1
	v_cvt_pk_bf16_f32 v1, v2, v3
	v_cvt_pk_bf16_f32 v2, v4, v5
	v_cvt_pk_bf16_f32 v3, v6, v7
	global_store_dwordx4 v[22:23], v[0:3], off
	global_load_dwordx4 v[0:3], v[28:29], off nt
	s_nop 0
	global_load_dwordx4 v[4:7], v[28:29], off offset:16 nt
	s_nop 0
	global_load_dword v28, v[14:15], off
	v_lshl_add_u64 v[14:15], v[24:25], 2, s[84:85]
	v_lshl_add_u64 v[22:23], v[8:9], 0, v[26:27]
	v_lshlrev_b32_e32 v24, 4, v32
	v_ashrrev_i32_e32 v25, 31, v24
	v_lshl_add_u64 v[24:25], v[24:25], 2, s[18:19]
	v_lshl_add_u64 v[24:25], v[24:25], 0, v[10:11]
	v_cmp_gt_u32_e64 s[12:13], v17, v37
	v_cmp_eq_u32_e64 s[14:15], 7, v33
	v_cmp_eq_u32_e64 s[16:17], v30, v16
	s_and_b64 s[0:1], s[0:1], s[16:17]
	s_and_b64 s[2:3], s[2:3], s[16:17]
	s_and_b64 s[4:5], s[4:5], s[16:17]
	s_and_b64 s[6:7], s[6:7], s[16:17]
	s_and_b64 s[8:9], s[8:9], s[16:17]
	s_and_b64 s[10:11], s[10:11], s[16:17]
	s_and_b64 s[14:15], s[14:15], s[16:17]
	s_and_b64 vcc, vcc, s[16:17]
	s_mov_b32 s20, 0xfffff
	s_waitcnt vmcnt(2)
; __device__ __forceinline__ unsigned pk2(float lo, float hi) { const f32x2h v = {lo, hi}; const bf16x2h b = __builtin_convertvector(v, bf16x2h); return __builtin_bit_cast(unsigned, b); }
; __device__ __forceinline__ void s5_tables1_ph(const int WID_, const float* dsk, const S5Tab& T) {
;     ...
;     for (int i = gtid; i < 32 * 512 * 64; i += gsz) {
;         const int c8 = i & 63, row = (i >> 6) & 511, g = i >> 15;
;         const int sp = row >> 4, hp = row & 15, s = c8 >> 1, h0 = (c8 & 1) * 8;
;         const bool on = s <= sp;
;         const float* k = T.Kmat + ((g * 32 + (on ? sp - s : 0)) * 16 + hp) * 16 + h0;
;         const float4 a = *(const float4*)k, b = *(const float4*)(k + 4);
;         const float dd = dsk[g * 16 + hp];
;         float v[8] = {a.x, a.y, a.z, a.w, b.x, b.y, b.z, b.w};
; #pragma unroll
;         for (int e = 0; e < 8; ++e) { if (!on) v[e] = 0.f; if ((row >> 3) == c8 && (row & 7) == e) v[e] += dd; }
;         *(uint4*)(T.BtA + ((size_t)g * 768 + row) * 512 + c8 * 8) = make_uint4(pk2(v[0], v[1]), pk2(v[2], v[3]), pk2(v[4], v[5]), pk2(v[6], v[7]));
;     }
	v_cndmask_b32_e64 v0, v0, 0, s[30:31]
	v_cndmask_b32_e64 v1, v1, 0, s[30:31]
	v_cndmask_b32_e64 v2, v2, 0, s[30:31]
	v_cndmask_b32_e64 v3, v3, 0, s[30:31]
	s_waitcnt vmcnt(1)
	v_cndmask_b32_e64 v4, v4, 0, s[30:31]
	v_cndmask_b32_e64 v5, v5, 0, s[30:31]
	v_cndmask_b32_e64 v6, v6, 0, s[30:31]
	v_cndmask_b32_e64 v7, v7, 0, s[30:31]
	s_waitcnt vmcnt(0)
	v_add_f32_e32 v26, v28, v0
	v_add_f32_e32 v27, v28, v1
	v_add_f32_e32 v29, v28, v2
	v_add_f32_e32 v32, v28, v3
	v_add_f32_e32 v34, v28, v4
	v_add_f32_e32 v35, v28, v5
	v_add_f32_e32 v38, v28, v6
	v_add_f32_e32 v28, v28, v7
	v_cndmask_b32_e64 v0, v0, v26, s[34:35]
	v_cndmask_b32_e64 v1, v1, v27, s[36:37]
	v_cndmask_b32_e64 v2, v2, v29, s[38:39]
	v_cndmask_b32_e64 v3, v3, v32, s[40:41]
	v_cndmask_b32_e64 v4, v4, v34, s[42:43]
	v_cndmask_b32_e64 v5, v5, v35, s[44:45]
	v_cndmask_b32_e64 v6, v6, v38, s[46:47]
	v_cndmask_b32_e64 v7, v7, v28, s[48:49]
	v_cvt_pk_bf16_f32 v0, v0, v1
	v_cvt_pk_bf16_f32 v1, v2, v3
	v_cvt_pk_bf16_f32 v2, v4, v5
	v_cvt_pk_bf16_f32 v3, v6, v7
	global_store_dwordx4 v[22:23], v[0:3], off
	global_load_dwordx4 v[4:7], v[24:25], off nt
	s_nop 0
	global_load_dwordx4 v[0:3], v[24:25], off offset:16 nt
	global_load_dword v22, v[14:15], off
	v_add_u32_e32 v23, s96, v31
	v_bfe_u32 v26, v20, 4, 5
	v_mul_i32_i24_e32 v14, 0x300, v36
	v_ashrrev_i32_e32 v27, 15, v23
	v_sub_u32_e64 v24, v26, v17 clamp
	v_ashrrev_i32_e32 v15, 31, v14
	v_lshlrev_b32_e32 v25, 9, v27
	v_lshlrev_b32_e32 v28, 4, v24
	v_lshl_add_u64 v[12:13], v[14:15], 0, v[12:13]
	v_or3_b32 v14, v28, v25, v21
	v_lshlrev_b32_e32 v14, 4, v14
	v_ashrrev_i32_e32 v15, 31, v14
	v_lshl_add_u64 v[14:15], v[14:15], 2, s[18:19]
	v_lshl_or_b32 v24, v27, 4, v21
	v_lshl_add_u64 v[14:15], v[14:15], 0, v[10:11]
	v_lshlrev_b64 v[12:13], 10, v[12:13]
	v_lshl_add_u64 v[12:13], v[8:9], 0, v[12:13]
	v_ashrrev_i32_e32 v25, 31, v24
	v_lshl_add_u64 v[24:25], v[24:25], 2, s[84:85]
	s_waitcnt vmcnt(2)
	v_cndmask_b32_e64 v4, v4, 0, s[12:13]
	v_cndmask_b32_e64 v5, v5, 0, s[12:13]
	v_cndmask_b32_e64 v6, v6, 0, s[12:13]
	v_cndmask_b32_e64 v7, v7, 0, s[12:13]
	s_waitcnt vmcnt(1)
	v_cndmask_b32_e64 v0, v0, 0, s[12:13]
	v_cndmask_b32_e64 v1, v1, 0, s[12:13]
	v_cndmask_b32_e64 v2, v2, 0, s[12:13]
	v_cndmask_b32_e64 v3, v3, 0, s[12:13]
	s_waitcnt vmcnt(0)
	v_add_f32_e32 v10, v22, v4
	v_add_f32_e32 v21, v22, v5
	v_add_f32_e32 v28, v22, v6
	v_add_f32_e32 v29, v22, v7
	v_add_f32_e32 v30, v22, v0
	v_add_f32_e32 v31, v22, v1
	v_add_f32_e32 v32, v22, v2
	v_add_f32_e32 v22, v22, v3
	v_cndmask_b32_e32 v4, v4, v10, vcc
	v_cndmask_b32_e64 v5, v5, v21, s[0:1]
	v_cndmask_b32_e64 v6, v6, v28, s[2:3]
	v_cndmask_b32_e64 v7, v7, v29, s[4:5]
	v_cndmask_b32_e64 v10, v0, v30, s[6:7]
	v_cndmask_b32_e64 v21, v1, v31, s[8:9]
	v_cndmask_b32_e64 v28, v2, v32, s[10:11]
	v_cndmask_b32_e64 v3, v3, v22, s[14:15]
	v_cvt_pk_bf16_f32 v0, v4, v5
	v_cvt_pk_bf16_f32 v1, v6, v7
	v_cvt_pk_bf16_f32 v2, v10, v21
	v_cvt_pk_bf16_f32 v3, v28, v3
	global_store_dwordx4 v[12:13], v[0:3], off
	global_load_dwordx4 v[4:7], v[14:15], off nt
	s_nop 0
	global_load_dwordx4 v[12:15], v[14:15], off offset:16 nt
	s_nop 0
	global_load_dword v3, v[24:25], off
	v_bfe_u32 v2, v19, 6, 3
	v_bfe_u32 v10, v20, 3, 6
	v_cmp_gt_u32_e32 vcc, v17, v26
	v_mul_i32_i24_e32 v20, 0x300, v27
	v_mov_b32_e32 v1, v11
	v_bfe_u32 v0, v19, 6, 9
	v_cmp_eq_u32_e64 s[0:1], 0, v2
	v_cmp_eq_u32_e64 s[2:3], 1, v2
	v_cmp_eq_u32_e64 s[4:5], 2, v2
	v_cmp_eq_u32_e64 s[6:7], 3, v2
	v_cmp_eq_u32_e64 s[8:9], 4, v2
	v_cmp_eq_u32_e64 s[10:11], 5, v2
	v_cmp_eq_u32_e64 s[12:13], 6, v2
	v_cmp_eq_u32_e64 s[14:15], 7, v2
	v_cmp_eq_u32_e64 s[16:17], v10, v16
	v_ashrrev_i32_e32 v21, 31, v20
	v_add_u32_e32 v2, s96, v23
	s_and_b64 s[2:3], s[2:3], s[16:17]
	s_and_b64 s[4:5], s[4:5], s[16:17]
	s_and_b64 s[6:7], s[6:7], s[16:17]
	s_and_b64 s[8:9], s[8:9], s[16:17]
	s_and_b64 s[10:11], s[10:11], s[16:17]
	s_and_b64 s[12:13], s[12:13], s[16:17]
	s_and_b64 s[14:15], s[14:15], s[16:17]
	s_and_b64 s[0:1], s[0:1], s[16:17]
	v_lshl_add_u64 v[0:1], v[20:21], 0, v[0:1]
	v_cmp_lt_i32_e64 s[20:21], s20, v2
	v_lshlrev_b64 v[0:1], 10, v[0:1]
	s_or_b64 s[62:63], s[20:21], s[62:63]
	v_lshl_add_u64 v[0:1], v[8:9], 0, v[0:1]
	s_waitcnt vmcnt(2)
	v_cndmask_b32_e64 v4, v4, 0, vcc
	v_cndmask_b32_e64 v5, v5, 0, vcc
	v_cndmask_b32_e64 v6, v6, 0, vcc
	v_cndmask_b32_e64 v7, v7, 0, vcc
	s_waitcnt vmcnt(1)
	v_cndmask_b32_e64 v10, v12, 0, vcc
	v_cndmask_b32_e64 v12, v13, 0, vcc
	v_cndmask_b32_e64 v13, v14, 0, vcc
	v_cndmask_b32_e64 v14, v15, 0, vcc
	s_waitcnt vmcnt(0)
	v_add_f32_e32 v15, v3, v4
	v_add_f32_e32 v19, v3, v5
	v_add_f32_e32 v20, v3, v6
	v_add_f32_e32 v21, v3, v7
	v_add_f32_e32 v22, v3, v10
	v_add_f32_e32 v23, v3, v12
	v_add_f32_e32 v24, v3, v13
	v_add_f32_e32 v3, v3, v14
	v_cndmask_b32_e64 v4, v4, v15, s[0:1]
	v_cndmask_b32_e64 v5, v5, v19, s[2:3]
	v_cndmask_b32_e64 v6, v6, v20, s[4:5]
	v_cndmask_b32_e64 v7, v7, v21, s[6:7]
	v_cndmask_b32_e64 v10, v10, v22, s[8:9]
	v_cndmask_b32_e64 v12, v12, v23, s[10:11]
	v_cndmask_b32_e64 v13, v13, v24, s[12:13]
	v_cndmask_b32_e64 v3, v14, v3, s[14:15]
	v_cvt_pk_bf16_f32 v4, v4, v5
	v_cvt_pk_bf16_f32 v5, v6, v7
	v_cvt_pk_bf16_f32 v6, v10, v12
	v_cvt_pk_bf16_f32 v7, v13, v3
	global_store_dwordx4 v[0:1], v[4:7], off
	s_andn2_b64 exec, exec, s[62:63]
	s_cbranch_execnz .LBB0_102

; __device__ __forceinline__ void final_ph(const int WID_, const bf16* __restrict__ x3, float* __restrict__ out, const bf16* __restrict__ yslot, const int* __restrict__ tok_slot, const float* __restrict__ w) {
;     ...
;     for (int row0 = (GB * 8 + wv) * 2; row0 < M; row0 += GN * 16) {
;         float4 v[2][4]; uint2 xa[2][4], ya[2][4], yb[2][4];
; #pragma unroll
;         for (int r = 0; r < 2; ++r) { const int row = row0 + r;
;             const uint2* xr = (const uint2*)(x3 + (size_t)row * D);
;             const uint2* pa = (const uint2*)(yslot + (size_t)tok_slot[2 * row] * D);
;             const uint2* pb = (const uint2*)(yslot + (size_t)tok_slot[2 * row + 1] * D);
; #pragma unroll
;             for (int j = 0; j < 4; ++j) { xa[r][j] = xr[lane + 64 * j]; ya[r][j] = pa[lane + 64 * j]; yb[r][j] = pb[lane + 64 * j]; } }
; #pragma unroll
;         for (int r = 0; r < 2; ++r) { float s = 0.f;
; #pragma unroll
;             for (int j = 0; j < 4; ++j) { const uint2 a = ya[r][j], b = yb[r][j], x = xa[r][j];
;                 v[r][j] = make_float4(__builtin_bit_cast(float, x.x << 16), __builtin_bit_cast(float, x.x & 0xffff0000u), __builtin_bit_cast(float, x.y << 16), __builtin_bit_cast(float, x.y & 0xffff0000u));
;                 v[r][j].x += __builtin_bit_cast(float, a.x << 16) + __builtin_bit_cast(float, b.x << 16);
;                 v[r][j].y += __builtin_bit_cast(float, a.x & 0xffff0000u) + __builtin_bit_cast(float, b.x & 0xffff0000u);
;                 v[r][j].z += __builtin_bit_cast(float, a.y << 16) + __builtin_bit_cast(float, b.y << 16);
;                 v[r][j].w += __builtin_bit_cast(float, a.y & 0xffff0000u) + __builtin_bit_cast(float, b.y & 0xffff0000u);
;                 s += v[r][j].x * v[r][j].x + v[r][j].y * v[r][j].y + v[r][j].z * v[r][j].z + v[r][j].w * v[r][j].w; }
.LBB0_2423:
	s_ashr_i32 s3, s2, 31
	s_lshl_b64 s[0:1], s[2:3], 2
	s_add_u32 s0, s12, s0
	s_addc_u32 s1, s13, s1
	global_load_dwordx2 v[24:25], v[20:21], off offset:-3584 nt
	global_load_dwordx2 v[28:29], v[20:21], off offset:-3072 nt
	global_load_dwordx2 v[26:27], v[20:21], off offset:-2560 nt
	global_load_dwordx2 v[22:23], v[20:21], off offset:-2048 nt
	global_load_dwordx2 v[30:31], v[20:21], off offset:-1536 nt
	global_load_dwordx2 v[36:37], v[20:21], off offset:-1024 nt
	global_load_dwordx2 v[34:35], v[20:21], off offset:-512 nt
	global_load_dwordx2 v[32:33], v[20:21], off nt
	v_mov_b32_e32 v41, 0
	v_mov_b32_e32 v123, 0
	v_mov_b32_e32 v122, 0
	v_mov_b32_e32 v124, 0
	s_add_i32 s4, s4, s6
	s_add_i32 s2, s2, s14
	v_lshl_add_u64 v[20:21], v[20:21], 0, s[10:11]
	s_waitcnt vmcnt(7)
	v_lshlrev_b32_e32 v46, 16, v24
	v_and_b32_e32 v47, 0xffff0000, v24
	s_waitcnt vmcnt(6)
	v_lshlrev_b32_e32 v48, 16, v28
	v_and_b32_e32 v49, 0xffff0000, v28
	s_waitcnt vmcnt(5)
	v_lshlrev_b32_e32 v50, 16, v26
	v_and_b32_e32 v51, 0xffff0000, v26
	s_waitcnt vmcnt(0)
	v_mov_b32_e32 v42, v126
	v_mov_b32_e32 v43, v127
	v_mov_b32_e32 v44, v128
	v_mov_b32_e32 v45, v129
	v_ashrrev_i32_e32 v63, 31, v42
	v_mov_b32_e32 v62, v42
	v_ashrrev_i32_e32 v65, 31, v43
	v_mov_b32_e32 v64, v43
	v_ashrrev_i32_e32 v43, 31, v44
	v_mov_b32_e32 v42, v44
	v_ashrrev_i32_e32 v67, 31, v45
	v_mov_b32_e32 v66, v45
	v_lshlrev_b64 v[62:63], 11, v[62:63]
	v_lshlrev_b64 v[42:43], 11, v[42:43]
	v_lshlrev_b64 v[44:45], 11, v[64:65]
	v_lshlrev_b64 v[64:65], 11, v[66:67]
	v_lshl_add_u64 v[62:63], v[16:17], 0, v[62:63]
	v_lshl_add_u64 v[42:43], v[16:17], 0, v[42:43]
	v_lshl_add_u64 v[44:45], v[16:17], 0, v[44:45]
	v_lshl_add_u64 v[64:65], v[16:17], 0, v[64:65]
	global_load_dwordx2 v[66:67], v[62:63], off nt
	global_load_dwordx2 v[68:69], v[44:45], off nt
	global_load_dwordx2 v[70:71], v[62:63], off offset:512 nt
	global_load_dwordx2 v[72:73], v[44:45], off offset:512 nt
	global_load_dwordx2 v[74:75], v[62:63], off offset:1024 nt
	global_load_dwordx2 v[76:77], v[44:45], off offset:1024 nt
	global_load_dwordx2 v[78:79], v[62:63], off offset:1536 nt
	global_load_dwordx2 v[80:81], v[44:45], off offset:1536 nt
	global_load_dwordx2 v[82:83], v[42:43], off nt
	global_load_dwordx2 v[84:85], v[64:65], off nt
	global_load_dwordx2 v[86:87], v[42:43], off offset:512 nt
	global_load_dwordx2 v[88:89], v[64:65], off offset:512 nt
	global_load_dwordx2 v[90:91], v[42:43], off offset:1024 nt
	global_load_dwordx2 v[92:93], v[64:65], off offset:1024 nt
	global_load_dwordx2 v[94:95], v[42:43], off offset:1536 nt
	s_nop 0
	global_load_dwordx2 v[42:43], v[64:65], off offset:1536 nt
	s_ashr_i32 s3, s2, 31
	s_lshl_b64 s[98:99], s[2:3], 2
	s_add_u32 s98, s12, s98
	s_addc_u32 s99, s13, s99
	global_load_dwordx4 v[126:129], v38, s[98:99]
	s_cmp_lt_i32 s4, 0x10000
	v_lshlrev_b32_e32 v52, 16, v22
	v_and_b32_e32 v53, 0xffff0000, v22
	v_lshlrev_b32_e32 v54, 16, v30
	v_and_b32_e32 v55, 0xffff0000, v30
	v_lshlrev_b32_e32 v56, 16, v36
	v_and_b32_e32 v57, 0xffff0000, v36
	v_lshlrev_b32_e32 v58, 16, v34
	v_and_b32_e32 v59, 0xffff0000, v34
	v_lshlrev_b32_e32 v60, 16, v32
	v_and_b32_e32 v61, 0xffff0000, v32
	v_lshlrev_b32_e32 v32, 16, v33
	v_and_b32_e32 v33, 0xffff0000, v33
	v_lshlrev_b32_e32 v24, 16, v25
	v_and_b32_e32 v25, 0xffff0000, v25
	v_lshlrev_b32_e32 v28, 16, v29
	v_and_b32_e32 v29, 0xffff0000, v29
	v_lshlrev_b32_e32 v26, 16, v27
	v_and_b32_e32 v27, 0xffff0000, v27
	v_lshlrev_b32_e32 v22, 16, v23
	v_and_b32_e32 v23, 0xffff0000, v23
	v_lshlrev_b32_e32 v30, 16, v31
	v_and_b32_e32 v31, 0xffff0000, v31
	v_lshlrev_b32_e32 v36, 16, v37
	v_and_b32_e32 v37, 0xffff0000, v37
	v_lshlrev_b32_e32 v34, 16, v35
	v_and_b32_e32 v35, 0xffff0000, v35
	s_waitcnt vmcnt(16)
	v_lshlrev_b32_e32 v44, 16, v66
	s_waitcnt vmcnt(15)
	v_lshlrev_b32_e32 v62, 16, v68
	v_and_b32_e32 v45, 0xffff0000, v66
	v_and_b32_e32 v63, 0xffff0000, v68
	v_lshlrev_b32_e32 v64, 16, v67
	v_lshlrev_b32_e32 v66, 16, v69
	v_and_b32_e32 v65, 0xffff0000, v67
	v_and_b32_e32 v67, 0xffff0000, v69
	s_waitcnt vmcnt(14)
	v_lshlrev_b32_e32 v68, 16, v70
	s_waitcnt vmcnt(13)
	v_lshlrev_b32_e32 v96, 16, v72
	v_and_b32_e32 v69, 0xffff0000, v70
	v_and_b32_e32 v97, 0xffff0000, v72
	s_waitcnt vmcnt(12)
	v_lshlrev_b32_e32 v98, 16, v74
	s_waitcnt vmcnt(11)
	v_lshlrev_b32_e32 v100, 16, v76
	v_and_b32_e32 v99, 0xffff0000, v74
	v_and_b32_e32 v101, 0xffff0000, v76
	s_waitcnt vmcnt(10)
	v_lshlrev_b32_e32 v102, 16, v78
	s_waitcnt vmcnt(9)
	v_lshlrev_b32_e32 v104, 16, v80
	v_and_b32_e32 v103, 0xffff0000, v78
	v_and_b32_e32 v105, 0xffff0000, v80
	v_lshlrev_b32_e32 v78, 16, v79
	v_lshlrev_b32_e32 v80, 16, v81
	v_and_b32_e32 v79, 0xffff0000, v79
	v_and_b32_e32 v81, 0xffff0000, v81
	v_lshlrev_b32_e32 v74, 16, v75
	v_lshlrev_b32_e32 v76, 16, v77
	v_and_b32_e32 v75, 0xffff0000, v75
	v_and_b32_e32 v77, 0xffff0000, v77
	s_waitcnt vmcnt(8)
	v_lshlrev_b32_e32 v106, 16, v82
	s_waitcnt vmcnt(7)
	v_lshlrev_b32_e32 v108, 16, v84
	v_and_b32_e32 v107, 0xffff0000, v82
	v_and_b32_e32 v109, 0xffff0000, v84
	s_waitcnt vmcnt(6)
	v_lshlrev_b32_e32 v110, 16, v86
	s_waitcnt vmcnt(5)
	v_lshlrev_b32_e32 v112, 16, v88
	v_and_b32_e32 v111, 0xffff0000, v86
	v_and_b32_e32 v113, 0xffff0000, v88
	v_lshlrev_b32_e32 v86, 16, v87
	v_lshlrev_b32_e32 v88, 16, v89
	v_and_b32_e32 v87, 0xffff0000, v87
	v_and_b32_e32 v89, 0xffff0000, v89
	s_waitcnt vmcnt(4)
	v_lshlrev_b32_e32 v114, 16, v90
	s_waitcnt vmcnt(3)
	v_lshlrev_b32_e32 v116, 16, v92
	v_and_b32_e32 v115, 0xffff0000, v90
	v_and_b32_e32 v117, 0xffff0000, v92
	s_waitcnt vmcnt(2)
	v_lshlrev_b32_e32 v118, 16, v94
	s_waitcnt vmcnt(1)
; __device__ __forceinline__ void final_ph(const int WID_, const bf16* __restrict__ x3, float* __restrict__ out, const bf16* __restrict__ yslot, const int* __restrict__ tok_slot, const float* __restrict__ w) {
;     ...
;         for (int r = 0; r < 2; ++r) { float s = 0.f;
; #pragma unroll
;             for (int j = 0; j < 4; ++j) { const uint2 a = ya[r][j], b = yb[r][j], x = xa[r][j];
;                 v[r][j] = make_float4(__builtin_bit_cast(float, x.x << 16), __builtin_bit_cast(float, x.x & 0xffff0000u), __builtin_bit_cast(float, x.y << 16), __builtin_bit_cast(float, x.y & 0xffff0000u));
;                 v[r][j].x += __builtin_bit_cast(float, a.x << 16) + __builtin_bit_cast(float, b.x << 16);
;                 v[r][j].y += __builtin_bit_cast(float, a.x & 0xffff0000u) + __builtin_bit_cast(float, b.x & 0xffff0000u);
;                 v[r][j].z += __builtin_bit_cast(float, a.y << 16) + __builtin_bit_cast(float, b.y << 16);
;                 v[r][j].w += __builtin_bit_cast(float, a.y & 0xffff0000u) + __builtin_bit_cast(float, b.y & 0xffff0000u);
;                 s += v[r][j].x * v[r][j].x + v[r][j].y * v[r][j].y + v[r][j].z * v[r][j].z + v[r][j].w * v[r][j].w; }
	v_lshlrev_b32_e32 v120, 16, v42
	v_and_b32_e32 v119, 0xffff0000, v94
	v_and_b32_e32 v121, 0xffff0000, v42
	v_lshlrev_b32_e32 v94, 16, v95
	v_lshlrev_b32_e32 v42, 16, v43
	v_and_b32_e32 v95, 0xffff0000, v95
	v_and_b32_e32 v43, 0xffff0000, v43
	v_pk_add_f32 v[102:103], v[102:103], v[104:105]
	v_pk_add_f32 v[78:79], v[78:79], v[80:81]
	v_pk_add_f32 v[80:81], v[98:99], v[100:101]
	v_pk_add_f32 v[68:69], v[68:69], v[96:97]
	v_pk_add_f32 v[44:45], v[44:45], v[62:63]
	v_lshlrev_b32_e32 v70, 16, v71
	v_lshlrev_b32_e32 v72, 16, v73
	v_and_b32_e32 v71, 0xffff0000, v71
	v_and_b32_e32 v73, 0xffff0000, v73
	v_pk_add_f32 v[74:75], v[74:75], v[76:77]
	v_pk_add_f32 v[62:63], v[64:65], v[66:67]
	v_pk_add_f32 v[64:65], v[118:119], v[120:121]
	v_pk_add_f32 v[42:43], v[94:95], v[42:43]
	v_pk_add_f32 v[66:67], v[114:115], v[116:117]
	v_pk_add_f32 v[76:77], v[110:111], v[112:113]
	v_pk_add_f32 v[86:87], v[86:87], v[88:89]
	v_pk_add_f32 v[88:89], v[106:107], v[108:109]
	v_pk_add_f32 v[52:53], v[102:103], v[52:53]
	v_pk_add_f32 v[50:51], v[80:81], v[50:51]
	v_pk_add_f32 v[48:49], v[68:69], v[48:49]
	v_pk_add_f32 v[44:45], v[44:45], v[46:47]
	v_lshlrev_b32_e32 v82, 16, v83
	v_lshlrev_b32_e32 v84, 16, v85
	v_and_b32_e32 v83, 0xffff0000, v83
	v_and_b32_e32 v85, 0xffff0000, v85
	v_lshlrev_b32_e32 v90, 16, v91
	v_lshlrev_b32_e32 v92, 16, v93
	v_and_b32_e32 v91, 0xffff0000, v91
	v_and_b32_e32 v93, 0xffff0000, v93
	v_pk_add_f32 v[70:71], v[70:71], v[72:73]
	v_pk_add_f32 v[46:47], v[64:65], v[60:61]
	v_pk_add_f32 v[32:33], v[42:43], v[32:33]
	v_pk_add_f32 v[42:43], v[66:67], v[58:59]
	v_pk_add_f32 v[56:57], v[76:77], v[56:57]
	v_pk_add_f32 v[54:55], v[88:89], v[54:55]
	v_mov_b32_e32 v60, v51
	v_mov_b32_e32 v61, v53
	v_mov_b32_e32 v68, v45
	v_mov_b32_e32 v69, v49
	v_pk_add_f32 v[72:73], v[90:91], v[92:93]
	v_pk_add_f32 v[82:83], v[82:83], v[84:85]
	v_pk_add_f32 v[28:29], v[70:71], v[28:29]
	v_pk_add_f32 v[24:25], v[62:63], v[24:25]
	v_mov_b32_e32 v58, v50
	v_mov_b32_e32 v59, v52
	v_mov_b32_e32 v66, v44
	v_mov_b32_e32 v67, v48
	v_mov_b32_e32 v76, v43
	v_mov_b32_e32 v77, v47
	v_mov_b32_e32 v84, v55
	v_mov_b32_e32 v85, v57
	v_pk_mul_f32 v[60:61], v[60:61], v[60:61]
	v_pk_mul_f32 v[68:69], v[68:69], v[68:69]
	v_pk_add_f32 v[22:23], v[78:79], v[22:23]
	v_pk_add_f32 v[26:27], v[74:75], v[26:27]
	v_pk_add_f32 v[34:35], v[72:73], v[34:35]
	v_pk_add_f32 v[36:37], v[86:87], v[36:37]
	v_pk_add_f32 v[30:31], v[82:83], v[30:31]
	v_mov_b32_e32 v70, v24
	v_mov_b32_e32 v71, v28
	v_mov_b32_e32 v74, v42
	v_mov_b32_e32 v75, v46
	v_mov_b32_e32 v82, v54
	v_mov_b32_e32 v83, v56
	v_pk_mul_f32 v[76:77], v[76:77], v[76:77]
	v_pk_mul_f32 v[84:85], v[84:85], v[84:85]
	v_pk_fma_f32 v[58:59], v[58:59], v[58:59], v[60:61]
	v_pk_fma_f32 v[60:61], v[66:67], v[66:67], v[68:69]
	v_mov_b32_e32 v62, v26
	v_mov_b32_e32 v63, v22
	v_mov_b32_e32 v72, v25
	v_mov_b32_e32 v73, v29
	v_mov_b32_e32 v78, v34
	v_mov_b32_e32 v79, v32
	v_mov_b32_e32 v86, v30
	v_mov_b32_e32 v87, v36
	v_pk_fma_f32 v[66:67], v[74:75], v[74:75], v[76:77]
	v_pk_fma_f32 v[68:69], v[82:83], v[82:83], v[84:85]
	v_pk_fma_f32 v[60:61], v[70:71], v[70:71], v[60:61]
	v_mov_b32_e32 v64, v27
	v_mov_b32_e32 v65, v23
	v_mov_b32_e32 v88, v31
	v_mov_b32_e32 v89, v37
	v_pk_fma_f32 v[58:59], v[62:63], v[62:63], v[58:59]
	v_pk_fma_f32 v[62:63], v[78:79], v[78:79], v[66:67]
	v_pk_fma_f32 v[66:67], v[86:87], v[86:87], v[68:69]
	v_pk_fma_f32 v[60:61], v[72:73], v[72:73], v[60:61]
	v_mov_b32_e32 v80, v35
	v_mov_b32_e32 v81, v33
	v_pk_fma_f32 v[58:59], v[64:65], v[64:65], v[58:59]
	v_pk_fma_f32 v[64:65], v[88:89], v[88:89], v[66:67]
	v_add_f32_e32 v60, v60, v61
	v_pk_fma_f32 v[62:63], v[80:81], v[80:81], v[62:63]
	v_add_f32_e32 v61, v64, v65
	v_add_f32_e32 v58, v60, v58
	v_add_f32_e32 v60, v61, v62
	v_add_f32_e32 v58, v58, v59
	v_add_f32_e32 v59, v60, v63
; __device__ __forceinline__ void final_ph(const int WID_, const bf16* __restrict__ x3, float* __restrict__ out, const bf16* __restrict__ yslot, const int* __restrict__ tok_slot, const float* __restrict__ w) {
;     ...
;             s = wave_sum(s);
;             const float rs = rsqrtf(s * (1.f / D) + 1e-6f);
;             float4* xo = (float4*)(out + (size_t)(row0 + r) * D);
; #pragma unroll
;             for (int j = 0; j < 4; ++j) xo[lane + 64 * j] = make_float4(v[r][j].x * rs * g[j].x, v[r][j].y * rs * g[j].y, v[r][j].z * rs * g[j].z, v[r][j].w * rs * g[j].w); }
;     }
	s_nop 0
	v_add_f32_dpp v58, v58, v58 quad_perm:[1,0,3,2] row_mask:0xf bank_mask:0xf bound_ctrl:1
	v_add_f32_dpp v59, v59, v59 quad_perm:[1,0,3,2] row_mask:0xf bank_mask:0xf bound_ctrl:1
	s_nop 0
	v_add_f32_dpp v58, v58, v58 quad_perm:[2,3,0,1] row_mask:0xf bank_mask:0xf bound_ctrl:1
	v_add_f32_dpp v59, v59, v59 quad_perm:[2,3,0,1] row_mask:0xf bank_mask:0xf bound_ctrl:1
	s_nop 0
	v_add_f32_dpp v58, v58, v58 row_half_mirror row_mask:0xf bank_mask:0xf bound_ctrl:1
	v_add_f32_dpp v59, v59, v59 row_half_mirror row_mask:0xf bank_mask:0xf bound_ctrl:1
	s_nop 0
	v_add_f32_dpp v58, v58, v58 row_mirror row_mask:0xf bank_mask:0xf bound_ctrl:1
	v_add_f32_dpp v59, v59, v59 row_mirror row_mask:0xf bank_mask:0xf bound_ctrl:1
	s_nop 0
	v_mov_b32_dpp v41, v58 row_bcast:15 row_mask:0xa bank_mask:0xf
	v_mov_b32_dpp v123, v59 row_bcast:15 row_mask:0xa bank_mask:0xf
	v_add_f32_e32 v41, v58, v41
	v_add_f32_e32 v58, v59, v123
	s_nop 0
	v_mov_b32_dpp v122, v41 row_bcast:31 row_mask:0xc bank_mask:0xf
	v_mov_b32_dpp v124, v58 row_bcast:31 row_mask:0xc bank_mask:0xf
	v_add_f32_e32 v41, v41, v122
	v_add_f32_e32 v58, v58, v124
	v_readlane_b32 s0, v41, 63
	v_readlane_b32 s1, v58, 63
	s_nop 0
	v_fma_f32 v41, s0, v40, v39
	v_fma_f32 v58, s1, v40, v39
	v_mul_f32_e32 v59, 0x4b800000, v41
	v_cmp_gt_f32_e64 s[0:1], s5, v41
	v_mul_f32_e32 v60, 0x4b800000, v58
	v_cmp_gt_f32_e32 vcc, s5, v58
	v_cndmask_b32_e64 v41, v41, v59, s[0:1]
	v_rsq_f32_e32 v41, v41
	v_cndmask_b32_e32 v58, v58, v60, vcc
	v_rsq_f32_e32 v59, v58
	v_mul_f32_e32 v58, 0x45800000, v41
	v_cndmask_b32_e64 v58, v41, v58, s[0:1]
	v_mul_f32_e32 v60, 0x45800000, v59
	v_cndmask_b32_e32 v60, v59, v60, vcc
	v_pk_mul_f32 v[44:45], v[44:45], v[58:59] op_sel_hi:[1,0]
	v_pk_mul_f32 v[24:25], v[24:25], v[58:59] op_sel_hi:[1,0]
	v_pk_mul_f32 v[48:49], v[48:49], v[58:59] op_sel_hi:[1,0]
	v_pk_mul_f32 v[28:29], v[28:29], v[58:59] op_sel_hi:[1,0]
	v_pk_mul_f32 v[50:51], v[50:51], v[58:59] op_sel_hi:[1,0]
	v_pk_mul_f32 v[62:63], v[26:27], v[58:59] op_sel_hi:[1,0]
	v_pk_mul_f32 v[52:53], v[52:53], v[58:59] op_sel_hi:[1,0]
	v_pk_mul_f32 v[58:59], v[22:23], v[58:59] op_sel_hi:[1,0]
	v_pk_mul_f32 v[54:55], v[54:55], v[60:61] op_sel_hi:[1,0]
	v_pk_mul_f32 v[64:65], v[30:31], v[60:61] op_sel_hi:[1,0]
	v_pk_mul_f32 v[56:57], v[56:57], v[60:61] op_sel_hi:[1,0]
	v_pk_mul_f32 v[66:67], v[36:37], v[60:61] op_sel_hi:[1,0]
	v_pk_mul_f32 v[68:69], v[42:43], v[60:61] op_sel_hi:[1,0]
	v_pk_mul_f32 v[70:71], v[34:35], v[60:61] op_sel_hi:[1,0]
	v_pk_mul_f32 v[72:73], v[46:47], v[60:61] op_sel_hi:[1,0]
	v_pk_mul_f32 v[60:61], v[32:33], v[60:61] op_sel_hi:[1,0]
	v_pk_mul_f32 v[22:23], v[0:1], v[44:45]
	v_pk_mul_f32 v[24:25], v[2:3], v[24:25]
	v_pk_mul_f32 v[26:27], v[4:5], v[48:49]
	v_pk_mul_f32 v[28:29], v[6:7], v[28:29]
	v_pk_mul_f32 v[30:31], v[8:9], v[50:51]
	v_pk_mul_f32 v[32:33], v[10:11], v[62:63]
	v_pk_mul_f32 v[34:35], v[12:13], v[52:53]
	v_pk_mul_f32 v[36:37], v[14:15], v[58:59]
	v_pk_mul_f32 v[42:43], v[0:1], v[54:55]
	v_pk_mul_f32 v[44:45], v[2:3], v[64:65]
	v_pk_mul_f32 v[46:47], v[4:5], v[56:57]
	v_pk_mul_f32 v[48:49], v[6:7], v[66:67]
	v_pk_mul_f32 v[50:51], v[8:9], v[68:69]
	v_pk_mul_f32 v[52:53], v[10:11], v[70:71]
	v_pk_mul_f32 v[54:55], v[12:13], v[72:73]
	v_pk_mul_f32 v[56:57], v[14:15], v[60:61]
	global_store_dwordx4 v[18:19], v[22:25], off offset:-4096
	global_store_dwordx4 v[18:19], v[26:29], off offset:-3072
	global_store_dwordx4 v[18:19], v[30:33], off offset:-2048
	global_store_dwordx4 v[18:19], v[34:37], off offset:-1024
	global_store_dwordx4 v[18:19], v[42:45], off
	global_store_dwordx4 v[18:19], v[46:49], off offset:1024
	global_store_dwordx4 v[18:19], v[50:53], off offset:2048
	global_store_dwordx4 v[18:19], v[54:57], off offset:3072
	v_lshl_add_u64 v[18:19], v[18:19], 0, s[8:9]
	s_cbranch_scc1 .LBB0_2423
